# loop-invariant wait hoisted: the gate/up unit-loop head vmcnt(0) (needed only for the count load) moved in front of the loop, so wave 0 no longer waits for its signal atomics at each unit start
# speedup vs baseline: 1.0025x; 1.0025x over previous
; __device__ __forceinline__ int tid_opaque() { int t = threadIdx.x; asm volatile("" : "+v"(t)); return t; }
; __device__ __forceinline__ int vwg_id() { const int G = gridDim.x; return (G % 8 == 0) ? (int)((blockIdx.x % 8) * (G / 8) + blockIdx.x / 8) : (int)blockIdx.x; }
; __device__ __forceinline__ void phase_moe_gu(const Ptrs& p, LAS unsigned char* lds) {
;     const int* counts = (const int*)(p.ws + OFF_CTRL); const bf16_t* h2 = (const bf16_t*)(p.ws + OFF_HA); bf16_t* act = (bf16_t*)(p.ws + OFF_ACT);
;     const __amdgpu_buffer_rsrc_t ract = __builtin_amdgcn_make_buffer_rsrc((void*)act, 0, 0x7ffffff0, 0x00020000);
;     MoeUnit mu; const int cv = counts[tid_opaque() & 31];
;     for (int u = vwg_id(); moe_unit(cv, u, 16, mu); u += gridDim.x) {
.LBB0_1003:
	s_add_u32 s20, s30, 0x18248000
	s_addc_u32 s28, s31, 0
	s_and_b32 s21, s28, 0xffff
	s_mov_b32 s27, 0x20000
	s_mov_b32 s26, 0x7ffffff0
	s_and_b32 s37, s37, 0xffff
	s_movk_i32 s66, 0x6000
	s_mov_b32 s67, 0x80000
	s_mov_b32 s76, 0x82000
	s_mov_b32 s77, 0x84000
	s_mov_b32 s78, 0x86000
	s_mov_b32 s79, 0x88000
	s_mov_b32 s80, 0x8a000
	s_mov_b32 s81, 0x8c000
	s_mov_b32 s82, 0x8e000
	s_movk_i32 s83, 0xf80
	s_add_i32 s29, 0, 0x18000
	s_add_i32 s64, 0, 0x10400
	s_mov_b32 s84, 0xc0e00000
	v_mov_b32_e32 v2, 0
	v_mov_b32_e32 v214, 0x40e00000
	s_waitcnt vmcnt(0)
	s_branch .LBB0_1006

; __device__ __forceinline__ bool moe_unit(int cv, int u, int ntiles_n, MoeUnit& mu) {
;     int base = 0;
; #pragma unroll
;     for (int e = 0; e < E; ++e) { const int c = __builtin_amdgcn_readlane(cv, e), tm = (c + 255) >> 8, nu = tm * ntiles_n;
;         if (u < nu) { mu.e = e; mu.cnt = c; mu.base = base; mu.nt = u / tm; mu.mt = u - mu.nt * tm; mu.light = (mu.mt == tm - 1 && c - mu.mt * 256 <= 128) ? 1 : 0; return true; }
;         u -= nu; base += tm * 256; }
.LBB0_1006:
	v_readlane_b32 s6, v1, 0
	s_add_i32 s8, s6, 0xff
	s_ashr_i32 s7, s8, 8
	s_lshl_b32 s9, s7, 4
	s_cmp_ge_i32 s65, s9
	s_cselect_b64 s[4:5], -1, 0
	s_mov_b64 s[0:1], -1
	s_and_b64 vcc, exec, s[4:5]
	s_cbranch_vccz .LBB0_1009
	s_sub_i32 s2, s65, s9
	s_and_b32 s3, s8, 0xffffff00
	s_cbranch_execz .LBB0_1010
